# both gathers: the token's six row loads (row statistics + bf16 x row) fetched one token ahead into spare VGPRs; the full waits at each token top removed
# speedup vs baseline: 1.0270x; 1.0055x over previous
.Lgprio_f:
	v_add_u32_e32 v0, s6, v0
	v_cmp_gt_i32_e32 vcc, s87, v0
	s_and_saveexec_b64 s[6:7], vcc
	s_mov_b32 s18, 0x800000
	s_cbranch_execz .LBB0_765
	v_ashrrev_i32_e32 v1, 31, v0
	v_and_b32_e32 v2, 15, v3
	v_lshlrev_b64 v[34:35], 9, v[0:1]
	v_lshl_add_u64 v[4:5], s[94:95], 0, v[34:35]
	v_lshlrev_b32_e32 v144, 2, v2
	v_lshl_add_u64 v[4:5], v[4:5], 0, v[144:145]
	global_load_dword v92, v[4:5], off
	global_load_dword v122, v[4:5], off offset:64
	v_readlane_b32 s12, v255, 7
	v_readlane_b32 s13, v255, 8
	s_lshl_b64 s[8:9], s[12:13], 17
	s_add_u32 s8, s88, s8
	s_addc_u32 s9, s89, s9
	s_lshl_b64 s[14:15], s[12:13], 23
	v_readlane_b32 s12, v253, 29
	v_readlane_b32 s13, v253, 30
	s_add_u32 s12, s12, s14
	v_and_b32_e32 v28, 63, v3
	s_addc_u32 s13, s13, s15
	v_readlane_b32 s16, v253, 27
	v_lshlrev_b32_e32 v144, 3, v28
	v_readlane_b32 s17, v253, 28
	s_add_u32 s14, s16, s14
	v_lshl_add_u64 v[6:7], s[12:13], 0, v[144:145]
	s_addc_u32 s15, s17, s15
	v_lshl_add_u64 v[4:5], s[14:15], 0, v[144:145]
	s_load_dwordx2 s[10:11], s[10:11], 0xf0
	v_lshlrev_b32_e32 v144, 5, v28
	v_and_b32_e32 v1, 32, v3
	v_cmp_eq_u32_e64 s[40:41], 0, v1
	v_and_b32_e32 v1, 16, v3
	v_and_b32_e32 v93, 60, v3
	v_cmp_eq_u32_e64 s[42:43], 0, v1
	v_and_b32_e32 v1, 8, v3
	v_cmp_eq_u32_e64 s[44:45], 0, v1
	v_and_b32_e32 v1, 4, v3
	v_or_b32_e32 v34, v34, v93
	v_cmp_eq_u32_e64 s[46:47], 0, v1
	s_waitcnt vmcnt(0)
	v_readlane_b32 s12, v92, 0
	s_ashr_i32 s13, s12, 31
	s_lshl_b64 s[12:13], s[12:13], 9
	v_lshl_add_u64 v[8:9], v[4:5], 0, s[12:13]
	v_lshl_add_u64 v[10:11], v[6:7], 0, s[12:13]
	v_readlane_b32 s12, v92, 1
	s_ashr_i32 s13, s12, 31
	s_lshl_b64 s[12:13], s[12:13], 9
	v_lshl_add_u64 v[12:13], v[6:7], 0, s[12:13]
	global_load_dwordx2 v[8:9], v[8:9], off
	s_nop 0
	global_load_dwordx2 v[82:83], v[10:11], off
	global_load_dwordx2 v[80:81], v[12:13], off
	v_lshl_add_u64 v[10:11], v[4:5], 0, s[12:13]
	v_readlane_b32 s12, v92, 2
	s_ashr_i32 s13, s12, 31
	s_lshl_b64 s[12:13], s[12:13], 9
	v_lshl_add_u64 v[12:13], v[4:5], 0, s[12:13]
	v_lshl_add_u64 v[14:15], v[6:7], 0, s[12:13]
	v_readlane_b32 s12, v92, 3
	s_ashr_i32 s13, s12, 31
	s_lshl_b64 s[12:13], s[12:13], 9
	v_lshl_add_u64 v[16:17], v[6:7], 0, s[12:13]
	global_load_dwordx2 v[10:11], v[10:11], off
	s_nop 0
	global_load_dwordx2 v[12:13], v[12:13], off
	s_nop 0
	global_load_dwordx2 v[78:79], v[14:15], off
	global_load_dwordx2 v[76:77], v[16:17], off
	v_lshl_add_u64 v[14:15], v[4:5], 0, s[12:13]
	v_readlane_b32 s12, v92, 4
	s_ashr_i32 s13, s12, 31
	s_lshl_b64 s[12:13], s[12:13], 9
	v_lshl_add_u64 v[16:17], v[4:5], 0, s[12:13]
	v_lshl_add_u64 v[18:19], v[6:7], 0, s[12:13]
	v_readlane_b32 s12, v92, 5
	s_ashr_i32 s13, s12, 31
	s_lshl_b64 s[12:13], s[12:13], 9
	v_lshl_add_u64 v[20:21], v[6:7], 0, s[12:13]
	global_load_dwordx2 v[14:15], v[14:15], off
	s_nop 0
	global_load_dwordx2 v[16:17], v[16:17], off
	s_nop 0
	global_load_dwordx2 v[74:75], v[18:19], off
	global_load_dwordx2 v[70:71], v[20:21], off
	v_lshl_add_u64 v[18:19], v[4:5], 0, s[12:13]
	v_readlane_b32 s12, v92, 6
	s_ashr_i32 s13, s12, 31
	s_lshl_b64 s[12:13], s[12:13], 9
	v_lshl_add_u64 v[20:21], v[4:5], 0, s[12:13]
	v_lshl_add_u64 v[22:23], v[6:7], 0, s[12:13]
	v_readlane_b32 s12, v92, 7
	s_ashr_i32 s13, s12, 31
	s_lshl_b64 s[12:13], s[12:13], 9
	v_lshl_add_u64 v[24:25], v[6:7], 0, s[12:13]
	global_load_dwordx2 v[18:19], v[18:19], off
	s_nop 0
	global_load_dwordx2 v[20:21], v[20:21], off
	s_nop 0
	global_load_dwordx2 v[68:69], v[22:23], off
	global_load_dwordx2 v[64:65], v[24:25], off
	v_lshl_add_u64 v[22:23], v[4:5], 0, s[12:13]
	v_readlane_b32 s12, v92, 8
	s_ashr_i32 s13, s12, 31
	s_lshl_b64 s[12:13], s[12:13], 9
	v_lshl_add_u64 v[24:25], v[4:5], 0, s[12:13]
	v_lshl_add_u64 v[26:27], v[6:7], 0, s[12:13]
	v_readlane_b32 s12, v92, 9
	s_ashr_i32 s13, s12, 31
	s_lshl_b64 s[12:13], s[12:13], 9
	global_load_dwordx2 v[22:23], v[22:23], off
	s_nop 0
	global_load_dwordx2 v[24:25], v[24:25], off
	s_nop 0
	global_load_dwordx2 v[62:63], v[26:27], off
	v_lshl_add_u64 v[26:27], v[4:5], 0, s[12:13]
	global_load_dwordx2 v[38:39], v[26:27], off
	v_lshl_add_u64 v[26:27], v[6:7], 0, s[12:13]
	v_readlane_b32 s12, v92, 10
	s_ashr_i32 s13, s12, 31
	s_lshl_b64 s[12:13], s[12:13], 9
	global_load_dwordx2 v[66:67], v[26:27], off
	v_lshl_add_u64 v[26:27], v[4:5], 0, s[12:13]
	global_load_dwordx2 v[50:51], v[26:27], off
	v_lshl_add_u64 v[26:27], v[6:7], 0, s[12:13]
	v_readlane_b32 s12, v92, 11
	s_ashr_i32 s13, s12, 31
	s_lshl_b64 s[12:13], s[12:13], 9
	global_load_dwordx2 v[60:61], v[26:27], off
	v_lshl_add_u64 v[26:27], v[4:5], 0, s[12:13]
	global_load_dwordx2 v[48:49], v[26:27], off
	v_lshl_add_u64 v[26:27], v[6:7], 0, s[12:13]
	v_readlane_b32 s12, v92, 12
	s_ashr_i32 s13, s12, 31
	s_lshl_b64 s[12:13], s[12:13], 9
	global_load_dwordx2 v[58:59], v[26:27], off
	v_lshl_add_u64 v[26:27], v[4:5], 0, s[12:13]
	global_load_dwordx2 v[46:47], v[26:27], off
	v_lshl_add_u64 v[26:27], v[6:7], 0, s[12:13]
	v_readlane_b32 s12, v92, 13
	s_ashr_i32 s13, s12, 31
	s_lshl_b64 s[12:13], s[12:13], 9
	global_load_dwordx2 v[56:57], v[26:27], off
	v_lshl_add_u64 v[26:27], v[4:5], 0, s[12:13]
	global_load_dwordx2 v[44:45], v[26:27], off
	v_lshl_add_u64 v[26:27], v[6:7], 0, s[12:13]
	v_readlane_b32 s12, v92, 14
	s_ashr_i32 s13, s12, 31
	s_lshl_b64 s[12:13], s[12:13], 9
	global_load_dwordx2 v[54:55], v[26:27], off
	v_lshl_add_u64 v[26:27], v[4:5], 0, s[12:13]
	global_load_dwordx2 v[42:43], v[26:27], off
	v_lshl_add_u64 v[26:27], v[6:7], 0, s[12:13]
	v_readlane_b32 s12, v92, 15
	s_ashr_i32 s13, s12, 31
	s_lshl_b64 s[12:13], s[12:13], 9
	global_load_dwordx2 v[52:53], v[26:27], off
	v_lshl_add_u64 v[26:27], v[4:5], 0, s[12:13]
	global_load_dwordx2 v[40:41], v[26:27], off
	v_lshl_add_u64 v[26:27], v[6:7], 0, s[12:13]
	global_load_dwordx2 v[36:37], v[26:27], off
	v_readlane_b32 s12, v253, 15
	v_readlane_b32 s13, v253, 16
	s_nop 1
	v_lshl_add_u64 v[26:27], s[12:13], 0, v[144:145]
	v_readlane_b32 s12, v253, 13
	v_lshlrev_b32_e32 v144, 6, v28
	v_readlane_b32 s13, v253, 14
	s_waitcnt lgkmcnt(0)
	v_lshl_add_u64 v[30:31], s[10:11], 0, v[144:145]
	v_readlane_b32 s10, v253, 23
	v_lshl_add_u64 v[28:29], s[12:13], 0, v[144:145]
	v_readlane_b32 s12, v253, 2
	v_readlane_b32 s13, v253, 3
	v_readlane_b32 s11, v253, 24
	v_readlane_b32 s14, v253, 4
	v_lshl_add_u64 v[32:33], s[12:13], 0, v[144:145]
	v_lshl_add_u64 v[34:35], s[10:11], 0, v[34:35]
	s_mov_b64 s[10:11], 0
	v_lshlrev_b32_e32 v144, 2, v2
	v_readlane_b32 s15, v253, 5
	global_load_dwordx4 v[124:127], v[30:31], off
	global_load_dwordx4 v[128:131], v[30:31], off offset:16
	global_load_dwordx4 v[132:135], v[30:31], off offset:32
	global_load_dwordx4 v[136:139], v[30:31], off offset:48
	v_readfirstlane_b32 s62, v4
	v_readfirstlane_b32 s63, v5
	v_readfirstlane_b32 s64, v6
	v_readfirstlane_b32 s65, v7
	v_and_b32_e32 v121, 63, v175
	v_lshlrev_b32_e32 v121, 3, v121
	v_mov_b32_e32 v250, v0
	v_ashrrev_i32_e32 v251, 31, v250
	v_lshlrev_b64 v[250:251], 6, v[250:251]
	v_lshl_add_u64 v[4:5], s[96:97], 0, v[250:251]
	v_lshlrev_b64 v[250:251], 5, v[250:251]
	v_lshl_add_u64 v[250:251], v[26:27], 0, v[250:251]
	global_load_dwordx4 v[226:229], v[4:5], off
	global_load_dwordx4 v[230:233], v[4:5], off offset:16
	global_load_dwordx4 v[234:237], v[4:5], off offset:32
	global_load_dwordx4 v[238:241], v[250:251], off
	global_load_dwordx4 v[242:245], v[250:251], off offset:16
	global_load_dwordx4 v[246:249], v[4:5], off offset:48
	s_waitcnt vmcnt(0)
.LBB0_762:
	v_ashrrev_i32_e32 v1, 31, v0
	v_lshlrev_b64 v[2:3], 6, v[0:1]
	v_lshl_add_u64 v[2:3], s[96:97], 0, v[2:3]
	v_mov_b64_e32 v[84:85], v[226:227]
	v_mov_b64_e32 v[86:87], v[228:229]
	v_mov_b64_e32 v[88:89], v[230:231]
	v_mov_b64_e32 v[90:91], v[232:233]
	v_lshlrev_b64 v[72:73], 11, v[0:1]
	v_mov_b64_e32 v[94:95], v[234:235]
	v_mov_b64_e32 v[96:97], v[236:237]
	v_lshl_add_u64 v[72:73], v[26:27], 0, v[72:73]
	v_mov_b64_e32 v[98:99], v[238:239]
	v_mov_b64_e32 v[100:101], v[240:241]
	v_mov_b64_e32 v[102:103], v[242:243]
	v_mov_b64_e32 v[104:105], v[244:245]
	v_mov_b64_e32 v[106:107], v[246:247]
	v_mov_b64_e32 v[108:109], v[248:249]
	v_add_u32_e32 v250, s86, v0
	v_cmp_gt_i32_e32 vcc, s87, v250
	s_nop 1
	v_cndmask_b32_e32 v250, v0, v250, vcc
	v_ashrrev_i32_e32 v251, 31, v250
	v_lshlrev_b64 v[250:251], 6, v[250:251]
	v_lshl_add_u64 v[4:5], s[96:97], 0, v[250:251]
	v_lshlrev_b64 v[250:251], 5, v[250:251]
	v_lshl_add_u64 v[250:251], v[26:27], 0, v[250:251]
	global_load_dwordx4 v[226:229], v[4:5], off
	global_load_dwordx4 v[230:233], v[4:5], off offset:16
	global_load_dwordx4 v[234:237], v[4:5], off offset:32
	global_load_dwordx4 v[238:241], v[250:251], off
	global_load_dwordx4 v[242:245], v[250:251], off offset:16
	global_load_dwordx4 v[246:249], v[4:5], off offset:48
	s_mov_b32 s14, 0x42ee0000
	s_mov_b32 s58, 16
	v_mov_b32_e32 v2, v85
	v_mov_b32_e32 v3, v86
	v_mov_b32_e32 v72, v89
	v_mov_b32_e32 v73, v90
	v_mov_b32_e32 v85, v87
	v_mov_b32_e32 v89, v91
	v_mov_b32_e32 v86, v95
	v_mov_b32_e32 v90, v97
	v_lshlrev_b32_e32 v91, 16, v98
	v_pk_add_f32 v[2:3], v[2:3], v[84:85]
	v_pk_add_f32 v[72:73], v[72:73], v[88:89]
	v_pk_add_f32 v[84:85], v[94:95], v[86:87]
	v_pk_add_f32 v[86:87], v[96:97], v[90:91]
	v_pk_add_f32 v[2:3], v[2:3], v[2:3] op_sel:[0,1] op_sel_hi:[1,0]
	v_pk_add_f32 v[72:73], v[72:73], v[72:73] op_sel:[0,1] op_sel_hi:[1,0]
	v_mov_b32_e32 v85, v108
	v_mov_b32_e32 v87, v109
	v_mov_b32_e32 v3, v106
	v_mov_b32_e32 v73, v107
	v_pk_add_f32 v[84:85], v[84:85], v[86:87]
	v_pk_add_f32 v[2:3], v[2:3], v[72:73]
	v_and_b32_e32 v98, 0xffff0000, v98
	v_pk_add_f32 v[2:3], v[2:3], v[84:85]
	v_lshlrev_b32_e32 v110, 16, v99
	v_add_f32_e32 v2, v2, v3
	v_fmamk_f32 v2, v2, 0x3a800000, v191
	v_mul_f32_e32 v3, 0x4b800000, v2
	v_cmp_gt_f32_e32 vcc, s18, v2
	v_and_b32_e32 v99, 0xffff0000, v99
	v_lshlrev_b32_e32 v111, 16, v100
	v_cndmask_b32_e32 v2, v2, v3, vcc
	v_rsq_f32_e32 v2, v2
	v_and_b32_e32 v100, 0xffff0000, v100
	v_lshlrev_b32_e32 v112, 16, v101
	v_and_b32_e32 v101, 0xffff0000, v101
	v_mul_f32_e32 v84, 0x45800000, v2
	v_cndmask_b32_e32 v2, v2, v84, vcc
	v_lshlrev_b32_e32 v113, 16, v102
	v_and_b32_e32 v102, 0xffff0000, v102
	v_lshlrev_b32_e32 v114, 16, v103
	v_and_b32_e32 v103, 0xffff0000, v103
	v_lshlrev_b32_e32 v115, 16, v104
	v_and_b32_e32 v3, 0xffff0000, v104
	v_lshlrev_b32_e32 v72, 16, v105
	v_and_b32_e32 v73, 0xffff0000, v105
	v_mul_f32_e32 v84, v2, v91
	v_mul_f32_e32 v85, v2, v98
	v_mul_f32_e32 v86, v2, v110
	v_mul_f32_e32 v87, v2, v99
	v_mul_f32_e32 v88, v2, v111
	v_mul_f32_e32 v89, v2, v100
	v_mul_f32_e32 v90, v2, v112
	v_mul_f32_e32 v91, v2, v101
	v_mul_f32_e32 v95, v2, v113
	v_mul_f32_e32 v96, v2, v102
	v_mul_f32_e32 v97, v2, v114
	v_mul_f32_e32 v98, v2, v103
	v_mul_f32_e32 v99, v2, v115
	v_mul_f32_e32 v100, v2, v3
	v_mul_f32_e32 v72, v2, v72
	v_mul_f32_e32 v73, v2, v73
	v_max_f32_e64 v2, |v84|, |v85|
	v_max_f32_e64 v3, |v86|, |v87|
	v_max_f32_e64 v94, |v88|, |v89|
	v_max_f32_e64 v101, |v90|, |v91|
	v_max3_f32 v2, v2, 0, v3
	v_max_f32_e64 v102, |v95|, |v96|
	v_max_f32_e64 v103, |v97|, |v98|
	v_max3_f32 v2, v2, v94, v101
	v_max_f32_e64 v104, |v99|, |v100|
	v_max_f32_e64 v105, |v72|, |v73|
	v_max3_f32 v2, v2, v102, v103
	v_max3_f32 v2, v2, v104, v105
	v_mov_b32_e32 v3, v2
	s_nop 1
	v_permlane32_swap_b32 v3, v2
	v_add_u32_e32 v94, s86, v0
	v_cmp_gt_i32_e64 s[48:49], s87, v94
	s_waitcnt lgkmcnt(0)
	v_max_f32_e32 v3, v3, v3
	v_max_f32_e32 v2, v2, v3
	v_mov_b32_e32 v3, v2
	s_nop 1
	v_permlane16_swap_b32 v3, v2
	s_waitcnt lgkmcnt(0)
	v_max_f32_e32 v3, v3, v3
	v_max_f32_e32 v2, v2, v3
	s_nop 1
	v_mov_b32_dpp v3, v2 row_ror:8 row_mask:0xf bank_mask:0xf
	s_waitcnt lgkmcnt(0)
	v_max_f32_e32 v3, v3, v3
	v_max_f32_e32 v2, v2, v3
	s_nop 1
	v_mov_b32_dpp v3, v2 row_half_mirror row_mask:0xf bank_mask:0xf
	s_nop 1
	v_mov_b32_dpp v3, v3 quad_perm:[3,2,1,0] row_mask:0xf bank_mask:0xf
	s_waitcnt lgkmcnt(0)
	v_max_f32_e32 v3, v3, v3
	v_max_f32_e32 v2, v2, v3
	s_nop 1
	v_mov_b32_dpp v3, v2 quad_perm:[2,3,0,1] row_mask:0xf bank_mask:0xf
	s_waitcnt lgkmcnt(0)
	v_max_f32_e32 v3, v3, v3
	v_max_f32_e32 v101, v2, v3
	s_nop 1
	v_mov_b32_dpp v102, v101 quad_perm:[1,0,3,2] row_mask:0xf bank_mask:0xf
	v_lshlrev_b64 v[2:3], 10, v[0:1]
	v_lshlrev_b64 v[206:207], 2, v[2:3]
	v_lshl_add_u64 v[206:207], v[28:29], 0, v[206:207]
	global_load_dwordx4 v[208:211], v[206:207], off offset:48
	global_load_dwordx4 v[212:215], v[206:207], off offset:32
	global_load_dwordx4 v[216:219], v[206:207], off offset:16
	global_load_dwordx4 v[220:223], v[206:207], off
	s_waitcnt lgkmcnt(0)
	v_max_f32_e32 v1, v102, v102
	v_max_f32_e32 v101, v101, v1
	v_div_scale_f32 v1, s[12:13], v101, v101, s14
	v_rcp_f32_e32 v102, v1
	v_div_scale_f32 v103, vcc, s14, v101, s14
	s_movk_i32 s12, 0x3fff
	v_fma_f32 v104, -v1, v102, 1.0
	v_fmac_f32_e32 v102, v104, v102
	v_mul_f32_e32 v104, v103, v102
	v_fma_f32 v105, -v1, v104, v103
	v_fmac_f32_e32 v104, v105, v102
	v_fma_f32 v1, -v1, v104, v103
	v_div_fmas_f32 v1, v1, v102, v104
	v_div_fixup_f32 v1, v1, v101, s14
	v_cmp_lt_f32_e32 vcc, 0, v101
	v_cmp_lt_i32_e64 s[50:51], s12, v94
	s_or_b64 s[10:11], s[50:51], s[10:11]
	v_cndmask_b32_e32 v102, 0, v1, vcc
	v_mul_f32_e32 v1, v84, v102
	v_mul_f32_e32 v84, v85, v102
	v_mul_f32_e32 v85, v86, v102
	v_mul_f32_e32 v86, v87, v102
	v_rndne_f32_e32 v1, v1
	v_rndne_f32_e32 v84, v84
	v_mul_f32_e32 v87, v88, v102
	v_mul_f32_e32 v88, v89, v102
	v_rndne_f32_e32 v85, v85
	v_rndne_f32_e32 v86, v86
	v_cvt_i32_f32_e32 v1, v1
	v_cvt_i32_f32_e32 v84, v84
	v_rndne_f32_e32 v87, v87
	v_rndne_f32_e32 v88, v88
	v_cvt_i32_f32_e32 v85, v85
	v_cvt_i32_f32_e32 v86, v86
	v_cvt_i32_f32_e32 v87, v87
	v_cvt_i32_f32_e32 v88, v88
	v_mul_f32_e32 v89, v90, v102
	v_add_u32_e32 v90, 8, v1
	v_add_u32_e32 v104, 8, v84
	v_and_b32_e32 v103, 15, v1
	v_lshlrev_b32_e32 v105, 4, v84
	v_add_u32_e32 v1, v1, v84
	v_lshl_add_u32 v84, v85, 4, v196
	v_lshl_add_u32 v107, v86, 8, v200
	v_lshrrev_b32_e32 v90, 4, v90
	v_and_b32_e32 v104, 0xf0, v104
	v_lshl_add_u32 v109, v87, 12, v201
	v_lshl_add_u32 v111, v88, 16, v202
	v_and_b32_e32 v84, 0xf00, v84
	v_and_b32_e32 v107, 0xf000, v107
	v_and_or_b32 v90, v90, 15, v104
	v_lshlrev_b32_e32 v106, 8, v85
	v_add3_u32 v1, v1, v85, v86
	v_and_b32_e32 v85, 0xf0000, v109
	v_and_b32_e32 v109, 0xf00000, v111
	v_or3_b32 v84, v90, v84, v107
	v_lshlrev_b32_e32 v110, 16, v87
	v_or3_b32 v84, v84, v85, v109
	v_add3_u32 v85, v1, v87, v88
	v_mul_f32_e32 v87, v91, v102
	v_rndne_f32_e32 v89, v89
	v_rndne_f32_e32 v87, v87
	v_cvt_i32_f32_e32 v89, v89
	v_cvt_i32_f32_e32 v87, v87
	v_lshlrev_b32_e32 v108, 12, v86
	v_and_b32_e32 v105, 0xf0, v105
	v_lshl_add_u32 v1, v89, 20, v203
	v_lshl_add_u32 v90, v87, 24, v204
	v_and_b32_e32 v1, 0xf000000, v1
	v_and_b32_e32 v90, 0xf0000000, v90
	v_and_b32_e32 v106, 0xf00, v106
	v_or3_b32 v1, v84, v1, v90
	v_lshl_or_b32 v84, v87, 28, v103
	v_lshlrev_b32_e32 v112, 20, v88
	v_and_b32_e32 v108, 0xf000, v108
	v_and_b32_e32 v86, 0xf0000, v110
	v_lshlrev_b32_e32 v88, 24, v89
	v_or3_b32 v84, v84, v105, v106
	v_and_b32_e32 v110, 0xf00000, v112
	v_and_b32_e32 v88, 0xf000000, v88
	v_or3_b32 v84, v84, v108, v86
	v_or3_b32 v88, v84, v110, v88
	v_add3_u32 v84, v85, v89, v87
	v_mul_f32_e32 v85, v95, v102
	v_mul_f32_e32 v86, v96, v102
	v_rndne_f32_e32 v85, v85
	v_rndne_f32_e32 v86, v86
	v_cvt_i32_f32_e32 v85, v85
	v_cvt_i32_f32_e32 v86, v86
	v_mul_f32_e32 v95, v99, v102
	v_mul_f32_e32 v96, v100, v102
	v_add_u32_e32 v87, 8, v85
	v_add_u32_e32 v89, 8, v86
	v_lshrrev_b32_e32 v87, 4, v87
	v_and_b32_e32 v89, 0xf0, v89
	v_and_or_b32 v87, v87, 15, v89
	v_mul_f32_e32 v89, v97, v102
	v_lshlrev_b32_e32 v91, 4, v86
	v_add3_u32 v84, v84, v85, v86
	v_mul_f32_e32 v86, v98, v102
	v_rndne_f32_e32 v89, v89
	v_rndne_f32_e32 v86, v86
	v_cvt_i32_f32_e32 v89, v89
	v_cvt_i32_f32_e32 v86, v86
	v_rndne_f32_e32 v95, v95
	v_rndne_f32_e32 v96, v96
	v_mul_f32_e32 v72, v72, v102
	v_mul_f32_e32 v73, v73, v102
	v_cvt_i32_f32_e32 v95, v95
	v_cvt_i32_f32_e32 v96, v96
	v_rndne_f32_e32 v72, v72
	v_rndne_f32_e32 v73, v73
	v_cvt_i32_f32_e32 v72, v72
	v_cvt_i32_f32_e32 v73, v73
	v_add3_u32 v84, v84, v89, v86
	v_add3_u32 v84, v84, v95, v96
	v_and_b32_e32 v90, 15, v85
	v_add3_u32 v84, v84, v72, v73
	v_cvt_f32_i32_e32 v84, v84
	v_lshl_add_u32 v85, v89, 4, v196
	v_lshlrev_b32_e32 v89, 8, v89
	v_and_b32_e32 v97, 0xf00, v89
	v_mov_b32_e32 v98, v84
	s_nop 1
	v_permlane32_swap_b32 v98, v84
	v_lshl_add_u32 v89, v86, 8, v200
	v_and_b32_e32 v85, 0xf00, v85
	v_and_b32_e32 v89, 0xf000, v89
	v_or3_b32 v85, v87, v85, v89
	s_waitcnt lgkmcnt(0)
	v_add_f32_e32 v84, v98, v84
	v_mov_b32_e32 v87, v84
	s_nop 1
	v_permlane16_swap_b32 v87, v84
	v_lshl_add_u32 v89, v95, 12, v201
	v_lshl_add_u32 v98, v96, 16, v202
	v_and_b32_e32 v89, 0xf0000, v89
	v_and_b32_e32 v98, 0xf00000, v98
	s_waitcnt lgkmcnt(0)
	v_add_f32_e32 v84, v84, v87
	s_nop 1
	v_mov_b32_dpp v87, v84 row_ror:8 row_mask:0xf bank_mask:0xf
	v_or3_b32 v85, v85, v89, v98
	v_lshlrev_b32_e32 v89, 20, v96
	v_and_b32_e32 v96, 0xf00000, v89
	v_lshl_add_u32 v89, v72, 20, v203
	s_waitcnt lgkmcnt(0)
	v_add_f32_e32 v84, v84, v87
	s_nop 1
	v_mov_b32_dpp v87, v84 row_half_mirror row_mask:0xf bank_mask:0xf
	s_nop 1
	v_mov_b32_dpp v87, v87 quad_perm:[3,2,1,0] row_mask:0xf bank_mask:0xf
	v_lshl_add_u32 v98, v73, 24, v204
	v_and_b32_e32 v89, 0xf000000, v89
	v_and_b32_e32 v98, 0xf0000000, v98
	v_or3_b32 v89, v85, v89, v98
	s_waitcnt lgkmcnt(0)
	v_add_f32_e32 v84, v84, v87
	s_nop 1
	v_mov_b32_dpp v87, v84 quad_perm:[2,3,0,1] row_mask:0xf bank_mask:0xf
	v_and_b32_e32 v91, 0xf0, v91
	v_lshlrev_b32_e32 v86, 12, v86
	v_lshlrev_b32_e32 v95, 16, v95
	v_lshl_or_b32 v73, v73, 28, v90
	s_waitcnt lgkmcnt(0)
	v_add_f32_e32 v84, v84, v87
	s_nop 1
	v_mov_b32_dpp v85, v84 quad_perm:[1,0,3,2] row_mask:0xf bank_mask:0xf
	v_and_b32_e32 v86, 0xf000, v86
	v_and_b32_e32 v95, 0xf0000, v95
	v_lshlrev_b32_e32 v72, 24, v72
	v_or3_b32 v73, v73, v91, v97
	v_and_b32_e32 v72, 0xf000000, v72
	v_or3_b32 v73, v73, v86, v95
	v_or3_b32 v90, v73, v96, v72
	s_waitcnt lgkmcnt(0)
	v_add_f32_e32 v72, v84, v85
	v_mul_f32_e32 v91, 0x3c09ae41, v101
	v_mul_f32_e32 v95, 0.5, v72
	v_mov_b32_e32 v103, 0
	v_mov_b64_e32 v[72:73], v[34:35]
	v_mov_b32_e32 v102, 0
	v_mov_b32_e32 v101, 0
	v_mov_b32_e32 v100, 0
	v_mov_b32_e32 v99, 0
	v_mov_b32_e32 v98, 0
	v_mov_b32_e32 v97, 0
	v_mov_b32_e32 v96, 0

.Lgprio_l:
	v_add_u32_e32 v0, s6, v0
	v_cmp_gt_i32_e32 vcc, s87, v0
	s_and_saveexec_b64 s[6:7], vcc
	s_mov_b32 s12, 0x800000
	s_cbranch_execz .LBB0_772
	v_ashrrev_i32_e32 v1, 31, v0
	v_and_b32_e32 v2, 15, v3
	v_lshlrev_b64 v[4:5], 9, v[0:1]
	v_lshl_add_u64 v[8:9], s[94:95], 0, v[4:5]
	v_lshlrev_b32_e32 v144, 2, v2
	v_lshl_add_u64 v[8:9], v[8:9], 0, v[144:145]
	global_load_dword v96, v[8:9], off
	global_load_dword v122, v[8:9], off offset:64
	v_and_b32_e32 v6, 63, v3
	v_readlane_b32 s10, v253, 27
	v_lshlrev_b32_e32 v144, 3, v6
	v_readlane_b32 s11, v253, 28
	s_load_dwordx2 s[8:9], s[8:9], 0x10
	v_and_b32_e32 v1, 32, v3
	v_lshl_add_u64 v[16:17], s[10:11], 0, v[144:145]
	v_readlane_b32 s10, v253, 29
	v_readlane_b32 s11, v253, 30
	v_cmp_eq_u32_e64 s[40:41], 0, v1
	v_and_b32_e32 v1, 16, v3
	v_lshl_add_u64 v[18:19], s[10:11], 0, v[144:145]
	v_lshlrev_b32_e32 v144, 5, v6
	v_and_b32_e32 v97, 60, v3
	v_cmp_eq_u32_e64 s[42:43], 0, v1
	v_and_b32_e32 v1, 8, v3
	v_cmp_eq_u32_e64 s[44:45], 0, v1
	v_and_b32_e32 v1, 4, v3
	v_or_b32_e32 v4, v4, v97
	v_cmp_eq_u32_e64 s[46:47], 0, v1
	s_waitcnt vmcnt(0)
	v_readlane_b32 s10, v96, 0
	s_ashr_i32 s11, s10, 31
	s_lshl_b64 s[10:11], s[10:11], 9
	v_lshl_add_u64 v[8:9], v[16:17], 0, s[10:11]
	global_load_dwordx2 v[20:21], v[8:9], off
	v_lshl_add_u64 v[8:9], v[18:19], 0, s[10:11]
	v_readlane_b32 s10, v96, 1
	s_ashr_i32 s11, s10, 31
	s_lshl_b64 s[10:11], s[10:11], 9
	global_load_dwordx2 v[92:93], v[8:9], off
	v_lshl_add_u64 v[8:9], v[16:17], 0, s[10:11]
	global_load_dwordx2 v[22:23], v[8:9], off
	v_lshl_add_u64 v[8:9], v[18:19], 0, s[10:11]
	v_readlane_b32 s10, v96, 2
	s_ashr_i32 s11, s10, 31
	s_lshl_b64 s[10:11], s[10:11], 9
	global_load_dwordx2 v[90:91], v[8:9], off
	v_lshl_add_u64 v[8:9], v[16:17], 0, s[10:11]
	global_load_dwordx2 v[24:25], v[8:9], off
	v_lshl_add_u64 v[8:9], v[18:19], 0, s[10:11]
	v_readlane_b32 s10, v96, 3
	s_ashr_i32 s11, s10, 31
	s_lshl_b64 s[10:11], s[10:11], 9
	global_load_dwordx2 v[88:89], v[8:9], off
	v_lshl_add_u64 v[8:9], v[16:17], 0, s[10:11]
	global_load_dwordx2 v[26:27], v[8:9], off
	v_lshl_add_u64 v[8:9], v[18:19], 0, s[10:11]
	v_readlane_b32 s10, v96, 4
	s_ashr_i32 s11, s10, 31
	s_lshl_b64 s[10:11], s[10:11], 9
	global_load_dwordx2 v[86:87], v[8:9], off
	v_lshl_add_u64 v[8:9], v[16:17], 0, s[10:11]
	global_load_dwordx2 v[28:29], v[8:9], off
	v_lshl_add_u64 v[8:9], v[18:19], 0, s[10:11]
	v_readlane_b32 s10, v96, 5
	s_ashr_i32 s11, s10, 31
	s_lshl_b64 s[10:11], s[10:11], 9
	global_load_dwordx2 v[84:85], v[8:9], off
	v_lshl_add_u64 v[8:9], v[16:17], 0, s[10:11]
	global_load_dwordx2 v[30:31], v[8:9], off
	v_lshl_add_u64 v[8:9], v[18:19], 0, s[10:11]
	v_readlane_b32 s10, v96, 6
	s_ashr_i32 s11, s10, 31
	s_lshl_b64 s[10:11], s[10:11], 9
	global_load_dwordx2 v[82:83], v[8:9], off
	v_lshl_add_u64 v[8:9], v[16:17], 0, s[10:11]
	global_load_dwordx2 v[32:33], v[8:9], off
	v_lshl_add_u64 v[8:9], v[18:19], 0, s[10:11]
	v_readlane_b32 s10, v96, 7
	s_ashr_i32 s11, s10, 31
	s_lshl_b64 s[10:11], s[10:11], 9
	global_load_dwordx2 v[80:81], v[8:9], off
	v_lshl_add_u64 v[8:9], v[16:17], 0, s[10:11]
	global_load_dwordx2 v[34:35], v[8:9], off
	v_lshl_add_u64 v[8:9], v[18:19], 0, s[10:11]
	v_readlane_b32 s10, v96, 8
	s_ashr_i32 s11, s10, 31
	s_lshl_b64 s[10:11], s[10:11], 9
	global_load_dwordx2 v[78:79], v[8:9], off
	v_lshl_add_u64 v[8:9], v[16:17], 0, s[10:11]
	global_load_dwordx2 v[36:37], v[8:9], off
	v_lshl_add_u64 v[8:9], v[18:19], 0, s[10:11]
	v_readlane_b32 s10, v96, 9
	s_ashr_i32 s11, s10, 31
	s_lshl_b64 s[10:11], s[10:11], 9
	global_load_dwordx2 v[76:77], v[8:9], off
	v_lshl_add_u64 v[8:9], v[16:17], 0, s[10:11]
	global_load_dwordx2 v[38:39], v[8:9], off
	v_lshl_add_u64 v[8:9], v[18:19], 0, s[10:11]
	v_readlane_b32 s10, v96, 10
	s_ashr_i32 s11, s10, 31
	s_lshl_b64 s[10:11], s[10:11], 9
	global_load_dwordx2 v[70:71], v[8:9], off
	v_lshl_add_u64 v[8:9], v[16:17], 0, s[10:11]
	global_load_dwordx2 v[40:41], v[8:9], off
	v_lshl_add_u64 v[8:9], v[18:19], 0, s[10:11]
	v_readlane_b32 s10, v96, 11
	s_ashr_i32 s11, s10, 31
	s_lshl_b64 s[10:11], s[10:11], 9
	global_load_dwordx2 v[66:67], v[8:9], off
	v_lshl_add_u64 v[8:9], v[16:17], 0, s[10:11]
	global_load_dwordx2 v[60:61], v[8:9], off
	v_lshl_add_u64 v[8:9], v[18:19], 0, s[10:11]
	v_readlane_b32 s10, v96, 12
	s_ashr_i32 s11, s10, 31
	s_lshl_b64 s[10:11], s[10:11], 9
	global_load_dwordx2 v[72:73], v[8:9], off
	v_lshl_add_u64 v[8:9], v[16:17], 0, s[10:11]
	global_load_dwordx2 v[58:59], v[8:9], off
	v_lshl_add_u64 v[8:9], v[18:19], 0, s[10:11]
	v_readlane_b32 s10, v96, 13
	s_ashr_i32 s11, s10, 31
	s_lshl_b64 s[10:11], s[10:11], 9
	global_load_dwordx2 v[68:69], v[8:9], off
	v_lshl_add_u64 v[8:9], v[16:17], 0, s[10:11]
	global_load_dwordx2 v[56:57], v[8:9], off
	v_lshl_add_u64 v[8:9], v[18:19], 0, s[10:11]
	v_readlane_b32 s10, v96, 14
	s_ashr_i32 s11, s10, 31
	s_lshl_b64 s[10:11], s[10:11], 9
	global_load_dwordx2 v[64:65], v[8:9], off
	v_lshl_add_u64 v[8:9], v[16:17], 0, s[10:11]
	global_load_dwordx2 v[54:55], v[8:9], off
	v_lshl_add_u64 v[8:9], v[18:19], 0, s[10:11]
	v_readlane_b32 s10, v96, 15
	s_ashr_i32 s11, s10, 31
	s_lshl_b64 s[10:11], s[10:11], 9
	global_load_dwordx2 v[62:63], v[8:9], off
	v_lshl_add_u64 v[8:9], v[16:17], 0, s[10:11]
	global_load_dwordx2 v[52:53], v[8:9], off
	v_lshl_add_u64 v[8:9], v[18:19], 0, s[10:11]
	global_load_dwordx2 v[50:51], v[8:9], off
	v_readlane_b32 s10, v253, 15
	v_readlane_b32 s11, v253, 16
	s_nop 1
	v_lshl_add_u64 v[42:43], s[10:11], 0, v[144:145]
	v_lshlrev_b32_e32 v144, 6, v6
	s_waitcnt lgkmcnt(0)
	v_lshl_add_u64 v[6:7], s[8:9], 0, v[144:145]
	s_mov_b64 s[8:9], 0x1000
	v_readlane_b32 s10, v253, 13
	v_lshl_add_u64 v[46:47], v[6:7], 0, s[8:9]
	v_readlane_b32 s8, v253, 23
	v_readlane_b32 s11, v253, 14
	v_readlane_b32 s9, v253, 24
	s_nop 0
	v_lshl_add_u64 v[44:45], s[10:11], 0, v[144:145]
	v_lshl_add_u64 v[48:49], s[8:9], 0, v[4:5]
	s_mov_b64 s[8:9], 0
	v_lshlrev_b32_e32 v144, 2, v2
	v_readfirstlane_b32 s62, v16
	v_readfirstlane_b32 s63, v17
	v_readfirstlane_b32 s64, v18
	v_readfirstlane_b32 s65, v19
	v_and_b32_e32 v121, 63, v175
	v_lshlrev_b32_e32 v121, 3, v121
	v_mov_b32_e32 v250, v0
	v_ashrrev_i32_e32 v251, 31, v250
	v_lshlrev_b64 v[250:251], 6, v[250:251]
	v_lshl_add_u64 v[16:17], s[96:97], 0, v[250:251]
	v_lshlrev_b64 v[250:251], 5, v[250:251]
	v_lshl_add_u64 v[250:251], v[42:43], 0, v[250:251]
	global_load_dwordx4 v[226:229], v[16:17], off
	global_load_dwordx4 v[230:233], v[16:17], off offset:16
	global_load_dwordx4 v[234:237], v[16:17], off offset:32
	global_load_dwordx4 v[238:241], v[250:251], off
	global_load_dwordx4 v[242:245], v[250:251], off offset:16
	global_load_dwordx4 v[246:249], v[16:17], off offset:48
	s_waitcnt vmcnt(0)
.LBB0_769:
	v_ashrrev_i32_e32 v1, 31, v0
	v_lshlrev_b64 v[2:3], 6, v[0:1]
	v_lshl_add_u64 v[14:15], s[96:97], 0, v[2:3]
	v_mov_b64_e32 v[2:3], v[226:227]
	v_mov_b64_e32 v[4:5], v[228:229]
	v_mov_b64_e32 v[6:7], v[230:231]
	v_mov_b64_e32 v[8:9], v[232:233]
	v_lshlrev_b64 v[74:75], 11, v[0:1]
	v_mov_b64_e32 v[10:11], v[234:235]
	v_mov_b64_e32 v[12:13], v[236:237]
	v_lshl_add_u64 v[74:75], v[42:43], 0, v[74:75]
	v_mov_b64_e32 v[98:99], v[238:239]
	v_mov_b64_e32 v[100:101], v[240:241]
	v_mov_b64_e32 v[102:103], v[242:243]
	v_mov_b64_e32 v[104:105], v[244:245]
	v_mov_b64_e32 v[106:107], v[246:247]
	v_mov_b64_e32 v[108:109], v[248:249]
	v_add_u32_e32 v250, s86, v0
	v_cmp_gt_i32_e32 vcc, s87, v250
	s_nop 1
	v_cndmask_b32_e32 v250, v0, v250, vcc
	v_ashrrev_i32_e32 v251, 31, v250
	v_lshlrev_b64 v[250:251], 6, v[250:251]
	v_lshl_add_u64 v[16:17], s[96:97], 0, v[250:251]
	v_lshlrev_b64 v[250:251], 5, v[250:251]
	v_lshl_add_u64 v[250:251], v[42:43], 0, v[250:251]
	global_load_dwordx4 v[226:229], v[16:17], off
	global_load_dwordx4 v[230:233], v[16:17], off offset:16
	global_load_dwordx4 v[234:237], v[16:17], off offset:32
	global_load_dwordx4 v[238:241], v[250:251], off
	global_load_dwordx4 v[242:245], v[250:251], off offset:16
	global_load_dwordx4 v[246:249], v[16:17], off offset:48
	s_mov_b32 s56, 16
	v_mov_b32_e32 v14, v3
	v_mov_b32_e32 v15, v4
	v_mov_b32_e32 v94, v7
	v_mov_b32_e32 v95, v8
	v_mov_b32_e32 v3, v5
	v_mov_b32_e32 v7, v9
	v_mov_b32_e32 v4, v11
	v_mov_b32_e32 v8, v13
	v_pk_add_f32 v[2:3], v[14:15], v[2:3]
	v_pk_add_f32 v[6:7], v[94:95], v[6:7]
	v_pk_add_f32 v[4:5], v[10:11], v[4:5]
	v_pk_add_f32 v[8:9], v[12:13], v[8:9]
	v_pk_add_f32 v[2:3], v[2:3], v[2:3] op_sel:[0,1] op_sel_hi:[1,0]
	v_pk_add_f32 v[6:7], v[6:7], v[6:7] op_sel:[0,1] op_sel_hi:[1,0]
	v_mov_b32_e32 v5, v108
	v_mov_b32_e32 v9, v109
	v_mov_b32_e32 v3, v106
	v_mov_b32_e32 v7, v107
	v_pk_add_f32 v[4:5], v[4:5], v[8:9]
	v_pk_add_f32 v[2:3], v[2:3], v[6:7]
	v_lshlrev_b32_e32 v110, 16, v98
	v_pk_add_f32 v[2:3], v[2:3], v[4:5]
	v_and_b32_e32 v98, 0xffff0000, v98
	v_add_f32_e32 v2, v2, v3
	v_fmamk_f32 v2, v2, 0x3a800000, v191
	v_mul_f32_e32 v3, 0x4b800000, v2
	v_cmp_gt_f32_e32 vcc, s12, v2
	v_lshlrev_b32_e32 v111, 16, v99
	v_and_b32_e32 v99, 0xffff0000, v99
	v_cndmask_b32_e32 v2, v2, v3, vcc
	v_rsq_f32_e32 v2, v2
	v_lshlrev_b32_e32 v112, 16, v100
	v_and_b32_e32 v100, 0xffff0000, v100
	v_lshlrev_b32_e32 v113, 16, v101
	v_mul_f32_e32 v6, 0x45800000, v2
	v_cndmask_b32_e32 v2, v2, v6, vcc
	v_and_b32_e32 v101, 0xffff0000, v101
	v_lshlrev_b32_e32 v114, 16, v102
	v_and_b32_e32 v102, 0xffff0000, v102
	v_lshlrev_b32_e32 v115, 16, v103
	v_and_b32_e32 v103, 0xffff0000, v103
	v_lshlrev_b32_e32 v116, 16, v104
	v_and_b32_e32 v3, 0xffff0000, v104
	v_lshlrev_b32_e32 v4, 16, v105
	v_and_b32_e32 v5, 0xffff0000, v105
	v_mul_f32_e32 v6, v2, v110
	v_mul_f32_e32 v7, v2, v98
	v_mul_f32_e32 v8, v2, v111
	v_mul_f32_e32 v9, v2, v99
	v_mul_f32_e32 v10, v2, v112
	v_mul_f32_e32 v11, v2, v100
	v_mul_f32_e32 v12, v2, v113
	v_mul_f32_e32 v13, v2, v101
	v_mul_f32_e32 v14, v2, v114
	v_mul_f32_e32 v15, v2, v102
	v_mul_f32_e32 v94, v2, v115
	v_mul_f32_e32 v95, v2, v103
	v_mul_f32_e32 v99, v2, v116
	v_mul_f32_e32 v100, v2, v3
	v_mul_f32_e32 v4, v2, v4
	v_mul_f32_e32 v5, v2, v5
	v_max_f32_e64 v2, |v6|, |v7|
	v_max_f32_e64 v3, |v8|, |v9|
	v_max_f32_e64 v98, |v10|, |v11|
	v_max_f32_e64 v101, |v12|, |v13|
	v_max3_f32 v2, v2, 0, v3
	v_max_f32_e64 v102, |v14|, |v15|
	v_max_f32_e64 v103, |v94|, |v95|
	v_max3_f32 v2, v2, v98, v101
	v_max_f32_e64 v104, |v99|, |v100|
	v_max_f32_e64 v105, |v4|, |v5|
	v_max3_f32 v2, v2, v102, v103
	v_max3_f32 v2, v2, v104, v105
	v_mov_b32_e32 v3, v2
	s_nop 1
	v_permlane32_swap_b32 v3, v2
	s_mov_b32 s12, 0x42ee0000
	v_add_u32_e32 v98, s86, v0
	v_cmp_gt_i32_e64 s[48:49], s87, v98
	s_waitcnt lgkmcnt(0)
	v_max_f32_e32 v3, v3, v3
	v_max_f32_e32 v2, v2, v3
	v_mov_b32_e32 v3, v2
	s_nop 1
	v_permlane16_swap_b32 v3, v2
	s_waitcnt lgkmcnt(0)
	v_max_f32_e32 v3, v3, v3
	v_max_f32_e32 v2, v2, v3
	s_nop 1
	v_mov_b32_dpp v3, v2 row_ror:8 row_mask:0xf bank_mask:0xf
	s_waitcnt lgkmcnt(0)
	v_max_f32_e32 v3, v3, v3
	v_max_f32_e32 v2, v2, v3
	s_nop 1
	v_mov_b32_dpp v3, v2 row_half_mirror row_mask:0xf bank_mask:0xf
	s_nop 1
	v_mov_b32_dpp v3, v3 quad_perm:[3,2,1,0] row_mask:0xf bank_mask:0xf
	s_waitcnt lgkmcnt(0)
	v_max_f32_e32 v3, v3, v3
	v_max_f32_e32 v2, v2, v3
	s_nop 1
	v_mov_b32_dpp v3, v2 quad_perm:[2,3,0,1] row_mask:0xf bank_mask:0xf
	s_waitcnt lgkmcnt(0)
	v_max_f32_e32 v3, v3, v3
	v_max_f32_e32 v101, v2, v3
	s_nop 1
	v_mov_b32_dpp v102, v101 quad_perm:[1,0,3,2] row_mask:0xf bank_mask:0xf
	v_lshlrev_b64 v[2:3], 10, v[0:1]
	v_lshl_add_u64 v[206:207], v[2:3], 2, v[44:45]
	global_load_dwordx4 v[208:211], v[206:207], off offset:48
	global_load_dwordx4 v[212:215], v[206:207], off offset:32
	global_load_dwordx4 v[216:219], v[206:207], off offset:16
	global_load_dwordx4 v[220:223], v[206:207], off
	s_waitcnt lgkmcnt(0)
	v_max_f32_e32 v1, v102, v102
	v_max_f32_e32 v101, v101, v1
	v_div_scale_f32 v1, s[10:11], v101, v101, s12
	v_rcp_f32_e32 v102, v1
	v_div_scale_f32 v103, vcc, s12, v101, s12
	s_movk_i32 s10, 0x3fff
	v_fma_f32 v104, -v1, v102, 1.0
	v_fmac_f32_e32 v102, v104, v102
	v_mul_f32_e32 v104, v103, v102
	v_fma_f32 v105, -v1, v104, v103
	v_fmac_f32_e32 v104, v105, v102
	v_fma_f32 v1, -v1, v104, v103
	v_div_fmas_f32 v1, v1, v102, v104
	v_div_fixup_f32 v1, v1, v101, s12
	v_cmp_lt_f32_e32 vcc, 0, v101
	v_cmp_lt_i32_e64 s[50:51], s10, v98
	s_or_b64 s[8:9], s[50:51], s[8:9]
	v_cndmask_b32_e32 v102, 0, v1, vcc
	v_mul_f32_e32 v1, v6, v102
	v_mul_f32_e32 v6, v7, v102
	v_mul_f32_e32 v7, v8, v102
	v_mul_f32_e32 v8, v9, v102
	v_rndne_f32_e32 v1, v1
	v_rndne_f32_e32 v6, v6
	v_mul_f32_e32 v9, v10, v102
	v_mul_f32_e32 v10, v11, v102
	v_rndne_f32_e32 v7, v7
	v_rndne_f32_e32 v8, v8
	v_cvt_i32_f32_e32 v1, v1
	v_cvt_i32_f32_e32 v6, v6
	v_rndne_f32_e32 v9, v9
	v_rndne_f32_e32 v10, v10
	v_cvt_i32_f32_e32 v7, v7
	v_cvt_i32_f32_e32 v8, v8
	v_cvt_i32_f32_e32 v9, v9
	v_cvt_i32_f32_e32 v10, v10
	v_mul_f32_e32 v11, v12, v102
	v_add_u32_e32 v12, 8, v1
	v_add_u32_e32 v104, 8, v6
	v_and_b32_e32 v103, 15, v1
	v_lshlrev_b32_e32 v105, 4, v6
	v_add_u32_e32 v1, v1, v6
	v_lshl_add_u32 v6, v7, 4, v196
	v_lshl_add_u32 v107, v8, 8, v200
	v_lshrrev_b32_e32 v12, 4, v12
	v_and_b32_e32 v104, 0xf0, v104
	v_lshl_add_u32 v109, v9, 12, v201
	v_lshl_add_u32 v111, v10, 16, v202
	v_and_b32_e32 v6, 0xf00, v6
	v_and_b32_e32 v107, 0xf000, v107
	v_and_or_b32 v12, v12, 15, v104
	v_lshlrev_b32_e32 v106, 8, v7
	v_add3_u32 v1, v1, v7, v8
	v_and_b32_e32 v7, 0xf0000, v109
	v_and_b32_e32 v109, 0xf00000, v111
	v_or3_b32 v6, v12, v6, v107
	v_lshlrev_b32_e32 v110, 16, v9
	v_or3_b32 v6, v6, v7, v109
	v_add3_u32 v7, v1, v9, v10
	v_mul_f32_e32 v9, v13, v102
	v_rndne_f32_e32 v11, v11
	v_rndne_f32_e32 v9, v9
	v_cvt_i32_f32_e32 v11, v11
	v_cvt_i32_f32_e32 v9, v9
	v_lshlrev_b32_e32 v108, 12, v8
	v_and_b32_e32 v105, 0xf0, v105
	v_lshl_add_u32 v1, v11, 20, v203
	v_lshl_add_u32 v12, v9, 24, v204
	v_and_b32_e32 v1, 0xf000000, v1
	v_and_b32_e32 v12, 0xf0000000, v12
	v_and_b32_e32 v106, 0xf00, v106
	v_or3_b32 v1, v6, v1, v12
	v_lshl_or_b32 v6, v9, 28, v103
	v_lshlrev_b32_e32 v112, 20, v10
	v_and_b32_e32 v108, 0xf000, v108
	v_and_b32_e32 v8, 0xf0000, v110
	v_lshlrev_b32_e32 v10, 24, v11
	v_or3_b32 v6, v6, v105, v106
	v_and_b32_e32 v110, 0xf00000, v112
	v_and_b32_e32 v10, 0xf000000, v10
	v_or3_b32 v6, v6, v108, v8
	v_or3_b32 v10, v6, v110, v10
	v_add3_u32 v6, v7, v11, v9
	v_mul_f32_e32 v7, v14, v102
	v_mul_f32_e32 v8, v15, v102
	v_rndne_f32_e32 v7, v7
	v_rndne_f32_e32 v8, v8
	v_cvt_i32_f32_e32 v7, v7
	v_cvt_i32_f32_e32 v8, v8
	v_mul_f32_e32 v14, v99, v102
	v_mul_f32_e32 v15, v100, v102
	v_add_u32_e32 v9, 8, v7
	v_add_u32_e32 v11, 8, v8
	v_lshrrev_b32_e32 v9, 4, v9
	v_and_b32_e32 v11, 0xf0, v11
	v_and_or_b32 v9, v9, 15, v11
	v_mul_f32_e32 v11, v94, v102
	v_lshlrev_b32_e32 v13, 4, v8
	v_add3_u32 v6, v6, v7, v8
	v_mul_f32_e32 v8, v95, v102
	v_rndne_f32_e32 v11, v11
	v_rndne_f32_e32 v8, v8
	v_cvt_i32_f32_e32 v11, v11
	v_cvt_i32_f32_e32 v8, v8
	v_rndne_f32_e32 v14, v14
	v_rndne_f32_e32 v15, v15
	v_mul_f32_e32 v4, v4, v102
	v_mul_f32_e32 v5, v5, v102
	v_cvt_i32_f32_e32 v14, v14
	v_cvt_i32_f32_e32 v15, v15
	v_rndne_f32_e32 v4, v4
	v_rndne_f32_e32 v5, v5
	v_cvt_i32_f32_e32 v4, v4
	v_cvt_i32_f32_e32 v5, v5
	v_add3_u32 v6, v6, v11, v8
	v_add3_u32 v6, v6, v14, v15
	v_and_b32_e32 v12, 15, v7
	v_add3_u32 v6, v6, v4, v5
	v_cvt_f32_i32_e32 v6, v6
	v_lshl_add_u32 v7, v11, 4, v196
	v_lshlrev_b32_e32 v11, 8, v11
	v_and_b32_e32 v94, 0xf00, v11
	v_mov_b32_e32 v95, v6
	s_nop 1
	v_permlane32_swap_b32 v95, v6
	v_lshl_add_u32 v11, v8, 8, v200
	v_and_b32_e32 v7, 0xf00, v7
	v_and_b32_e32 v11, 0xf000, v11
	v_or3_b32 v7, v9, v7, v11
	s_waitcnt lgkmcnt(0)
	v_add_f32_e32 v6, v95, v6
	v_mov_b32_e32 v9, v6
	s_nop 1
	v_permlane16_swap_b32 v9, v6
	v_lshl_add_u32 v11, v14, 12, v201
	v_lshl_add_u32 v95, v15, 16, v202
	v_and_b32_e32 v11, 0xf0000, v11
	v_and_b32_e32 v95, 0xf00000, v95
	s_waitcnt lgkmcnt(0)
	v_add_f32_e32 v6, v6, v9
	s_nop 1
	v_mov_b32_dpp v9, v6 row_ror:8 row_mask:0xf bank_mask:0xf
	v_or3_b32 v7, v7, v11, v95
	v_lshlrev_b32_e32 v11, 20, v15
	v_and_b32_e32 v15, 0xf00000, v11
	v_lshl_add_u32 v11, v4, 20, v203
	s_waitcnt lgkmcnt(0)
	v_add_f32_e32 v6, v6, v9
	s_nop 1
	v_mov_b32_dpp v9, v6 row_half_mirror row_mask:0xf bank_mask:0xf
	s_nop 1
	v_mov_b32_dpp v9, v9 quad_perm:[3,2,1,0] row_mask:0xf bank_mask:0xf
	v_lshl_add_u32 v95, v5, 24, v204
	v_and_b32_e32 v11, 0xf000000, v11
	v_and_b32_e32 v95, 0xf0000000, v95
	v_or3_b32 v11, v7, v11, v95
	s_waitcnt lgkmcnt(0)
	v_add_f32_e32 v6, v6, v9
	s_nop 1
	v_mov_b32_dpp v9, v6 quad_perm:[2,3,0,1] row_mask:0xf bank_mask:0xf
	v_and_b32_e32 v13, 0xf0, v13
	v_lshlrev_b32_e32 v8, 12, v8
	v_lshlrev_b32_e32 v14, 16, v14
	v_lshl_or_b32 v5, v5, 28, v12
	s_waitcnt lgkmcnt(0)
	v_add_f32_e32 v6, v6, v9
	s_nop 1
	v_mov_b32_dpp v7, v6 quad_perm:[1,0,3,2] row_mask:0xf bank_mask:0xf
	v_and_b32_e32 v8, 0xf000, v8
	v_and_b32_e32 v14, 0xf0000, v14
	v_lshlrev_b32_e32 v4, 24, v4
	v_or3_b32 v5, v5, v13, v94
	v_and_b32_e32 v4, 0xf000000, v4
	v_or3_b32 v5, v5, v8, v14
	v_or3_b32 v12, v5, v15, v4
	s_waitcnt lgkmcnt(0)
	v_add_f32_e32 v4, v6, v7
	v_mul_f32_e32 v13, 0x3c09ae41, v101
	v_mul_f32_e32 v14, 0.5, v4
	v_mov_b32_e32 v105, 0
	v_mov_b64_e32 v[4:5], v[48:49]
	v_mov_b32_e32 v104, 0
	v_mov_b32_e32 v103, 0
	v_mov_b32_e32 v102, 0
	v_mov_b32_e32 v101, 0
	v_mov_b32_e32 v100, 0
	v_mov_b32_e32 v99, 0
	v_mov_b32_e32 v15, 0
